# v98 + k6 router finalize: the 16 partial-logit loads (4 serialized groups reusing registers) and the 6 constant loads issued together, sums in the original order
# speedup vs baseline: 1.0081x; 1.0020x over previous
.LBB0_1039:
	v_cmp_gt_i32_e64 s[38:39], 32, v28
	v_lshl_add_u32 v29, v28, 2, 0
	s_and_saveexec_b64 s[26:27], s[38:39]
	v_add_u32_e32 v2, 0x24040, v29
	ds_write_b32 v2, v67
	s_or_b64 exec, exec, s[26:27]
	s_ashr_i32 s3, s2, 6
	s_cmp_gt_i32 s3, 3
	s_waitcnt lgkmcnt(0)
	s_barrier
	s_cbranch_scc1 .LBB0_1065
	s_mov_b32 s49, s73
	s_lshl_b64 s[4:5], s[48:49], 2
	s_add_u32 s34, s44, s4
	s_addc_u32 s35, s45, s5
	s_lshl_b32 s2, s3, 4
	v_readlane_b32 s4, v254, 18
	v_and_b32_e32 v30, 15, v205
	s_add_i32 s4, s2, s4
	v_or_b32_e32 v2, s4, v30
	v_ashrrev_i32_e32 v3, 31, v2
	v_bfe_u32 v31, v205, 4, 2
	v_lshlrev_b64 v[2:3], 9, v[2:3]
	v_lshl_add_u64 v[2:3], s[44:45], 0, v[2:3]
	v_lshlrev_b32_e32 v66, 4, v31
	v_lshl_add_u64 v[2:3], v[2:3], 0, v[66:67]
	s_mov_b64 s[4:5], 0x26a00000
	v_lshl_add_u64 v[4:5], v[2:3], 0, s[4:5]
	s_mov_b32 s4, 0x26a00000
	v_add_co_u32_e32 v2, vcc, s4, v2
	s_mov_b64 s[4:5], 0xb80000
	s_nop 0
	v_addc_co_u32_e32 v3, vcc, 0, v3, vcc
	global_load_dwordx2 v[100:101], v[4:5], off sc1
	global_load_dwordx2 v[102:103], v[4:5], off offset:8 sc1
	global_load_dwordx2 v[104:105], v[4:5], off offset:64 sc1
	global_load_dwordx2 v[106:107], v[4:5], off offset:72 sc1
	global_load_dwordx2 v[108:109], v[4:5], off offset:128 sc1
	global_load_dwordx2 v[110:111], v[4:5], off offset:136 sc1
	global_load_dwordx2 v[112:113], v[4:5], off offset:192 sc1
	global_load_dwordx2 v[114:115], v[4:5], off offset:200 sc1
	global_load_dwordx2 v[116:117], v[4:5], off offset:256 sc1
	global_load_dwordx2 v[118:119], v[4:5], off offset:264 sc1
	global_load_dwordx2 v[120:121], v[4:5], off offset:320 sc1
	global_load_dwordx2 v[122:123], v[4:5], off offset:328 sc1
	global_load_dwordx2 v[124:125], v[4:5], off offset:384 sc1
	global_load_dwordx2 v[126:127], v[4:5], off offset:392 sc1
	global_load_dwordx2 v[128:129], v[4:5], off offset:448 sc1
	global_load_dwordx2 v[130:131], v[4:5], off offset:456 sc1
	s_lshl_b32 s3, s3, 7
	s_mov_b32 s6, 0x42ce8ed0
	s_mov_b32 s7, 0xc2b17218
	v_lshl_add_u64 v[10:11], s[34:35], 0, v[66:67]
	v_lshl_add_u64 v[12:13], v[10:11], 0, s[4:5]
	s_mov_b32 s4, 0xb80000
	v_add_co_u32_e32 v10, vcc, s4, v10
	s_nop 1
	v_addc_co_u32_e32 v11, vcc, 0, v11, vcc
	global_load_dwordx4 v[2:5], v66, s[46:47]
	global_load_dwordx4 v[6:9], v66, s[46:47] offset:64
	global_load_dwordx4 v[22:25], v[10:11], off
	global_load_dwordx4 v[18:21], v[12:13], off offset:64
	global_load_dwordx4 v[14:17], v[12:13], off offset:128
	s_nop 0
	global_load_dwordx4 v[10:13], v[12:13], off offset:192
	s_waitcnt vmcnt(6)
	v_add_f32_e32 v132, 0, v100
	v_add_f32_e32 v133, 0, v101
	v_add_f32_e32 v134, 0, v102
	v_add_f32_e32 v135, 0, v103
	v_add_f32_e32 v136, 0, v104
	v_add_f32_e32 v137, 0, v105
	v_add_f32_e32 v138, 0, v106
	v_add_f32_e32 v139, 0, v107
	v_add_f32_e32 v132, v132, v108
	v_add_f32_e32 v133, v133, v109
	v_add_f32_e32 v134, v134, v110
	v_add_f32_e32 v135, v135, v111
	v_add_f32_e32 v136, v136, v112
	v_add_f32_e32 v137, v137, v113
	v_add_f32_e32 v138, v138, v114
	v_add_f32_e32 v139, v139, v115
	v_add_f32_e32 v132, v132, v116
	v_add_f32_e32 v133, v133, v117
	v_add_f32_e32 v134, v134, v118
	v_add_f32_e32 v135, v135, v119
	v_add_f32_e32 v136, v136, v120
	v_add_f32_e32 v137, v137, v121
	v_add_f32_e32 v138, v138, v122
	v_add_f32_e32 v139, v139, v123
	v_add_f32_e32 v38, v132, v124
	v_add_f32_e32 v36, v133, v125
	v_add_f32_e32 v34, v134, v126
	v_add_f32_e32 v32, v135, v127
	v_add_f32_e32 v39, v136, v128
	v_add_f32_e32 v37, v137, v129
	v_add_f32_e32 v35, v138, v130
	v_add_f32_e32 v33, v139, v131
	v_readlane_b32 s4, v254, 19
	s_add_i32 s3, s4, s3
	v_lshl_add_u32 v26, v30, 3, s3
	ds_read_b64 v[26:27], v26
	s_mov_b32 s3, 0xbfb8aa3b
	s_waitcnt vmcnt(3) lgkmcnt(0)
	v_fma_f32 v22, -v22, v26, v38
	s_waitcnt vmcnt(2)
	v_fma_f32 v18, -v18, v26, v39
	s_waitcnt vmcnt(1)
	v_fma_f32 v14, v27, v22, v14
	s_waitcnt vmcnt(0)
	v_fma_f32 v18, v27, v18, v10
	v_mul_f32_e32 v10, 0xbfb8aa3b, v14
	v_fma_f32 v22, v14, s3, -v10
	v_rndne_f32_e32 v38, v10
	v_fmac_f32_e32 v22, 0xb2a5705f, v14
	v_sub_f32_e32 v10, v10, v38
	v_add_f32_e32 v10, v10, v22
	v_exp_f32_e32 v10, v10
	v_cvt_i32_f32_e32 v22, v38
	v_cmp_nlt_f32_e32 vcc, s6, v14
	v_ldexp_f32 v10, v10, v22
	s_nop 0
	v_cndmask_b32_e32 v10, 0, v10, vcc
	v_cmp_ngt_f32_e32 vcc, s7, v14
	s_nop 1
	v_cndmask_b32_e32 v10, v252, v10, vcc
	v_add_f32_e32 v10, 1.0, v10
	v_div_scale_f32 v14, s[4:5], v10, v10, 1.0
	v_rcp_f32_e32 v22, v14
	s_nop 0
	v_fma_f32 v38, -v14, v22, 1.0
	v_fmac_f32_e32 v22, v38, v22
	v_div_scale_f32 v38, vcc, 1.0, v10, 1.0
	v_mul_f32_e32 v39, v38, v22
	v_fma_f32 v40, -v14, v39, v38
	v_fmac_f32_e32 v39, v40, v22
	v_fma_f32 v14, -v14, v39, v38
	v_div_fmas_f32 v14, v14, v22, v39
	v_div_fixup_f32 v10, v14, v10, 1.0
	v_mul_f32_e32 v14, 0xbfb8aa3b, v18
	v_fma_f32 v22, v18, s3, -v14
	v_rndne_f32_e32 v38, v14
	v_fmac_f32_e32 v22, 0xb2a5705f, v18
	v_sub_f32_e32 v14, v14, v38
	v_add_f32_e32 v14, v14, v22
	v_exp_f32_e32 v14, v14
	v_cvt_i32_f32_e32 v22, v38
	v_cmp_nlt_f32_e32 vcc, s6, v18
	v_add_f32_e32 v2, v2, v10
	v_ldexp_f32 v14, v14, v22
	v_cndmask_b32_e32 v14, 0, v14, vcc
	v_cmp_ngt_f32_e32 vcc, s7, v18
	s_nop 1
	v_cndmask_b32_e32 v14, v252, v14, vcc
	v_add_f32_e32 v14, 1.0, v14
	v_div_scale_f32 v18, s[4:5], v14, v14, 1.0
	v_rcp_f32_e32 v22, v18
	s_nop 0
	v_fma_f32 v38, -v18, v22, 1.0
	v_fmac_f32_e32 v22, v38, v22
	v_div_scale_f32 v38, vcc, 1.0, v14, 1.0
	v_mul_f32_e32 v39, v38, v22
	v_fma_f32 v40, -v18, v39, v38
	v_fmac_f32_e32 v39, v40, v22
	v_fma_f32 v18, -v18, v39, v38
	v_div_fmas_f32 v18, v18, v22, v39
	v_div_fixup_f32 v14, v18, v14, 1.0
	v_fma_f32 v18, -v23, v26, v36
	v_fma_f32 v15, v27, v18, v15
	v_fma_f32 v18, -v19, v26, v37
	v_fma_f32 v18, v27, v18, v11
	v_mul_f32_e32 v11, 0xbfb8aa3b, v15
	v_fma_f32 v19, v15, s3, -v11
	v_rndne_f32_e32 v22, v11
	v_fmac_f32_e32 v19, 0xb2a5705f, v15
	v_sub_f32_e32 v11, v11, v22
	v_add_f32_e32 v11, v11, v19
	v_exp_f32_e32 v11, v11
	v_cvt_i32_f32_e32 v19, v22
	v_cmp_nlt_f32_e32 vcc, s6, v15
	v_add_f32_e32 v6, v6, v14
	v_ldexp_f32 v11, v11, v19
	v_cndmask_b32_e32 v11, 0, v11, vcc
	v_cmp_ngt_f32_e32 vcc, s7, v15
	s_nop 1
	v_cndmask_b32_e32 v11, v252, v11, vcc
	v_add_f32_e32 v11, 1.0, v11
	v_div_scale_f32 v15, s[4:5], v11, v11, 1.0
	v_rcp_f32_e32 v19, v15
	s_nop 0
	v_fma_f32 v22, -v15, v19, 1.0
	v_fmac_f32_e32 v19, v22, v19
	v_div_scale_f32 v22, vcc, 1.0, v11, 1.0
	v_mul_f32_e32 v23, v22, v19
	v_fma_f32 v36, -v15, v23, v22
	v_fmac_f32_e32 v23, v36, v19
	v_fma_f32 v15, -v15, v23, v22
	v_div_fmas_f32 v15, v15, v19, v23
	v_div_fixup_f32 v11, v15, v11, 1.0
	v_mul_f32_e32 v15, 0xbfb8aa3b, v18
	v_fma_f32 v19, v18, s3, -v15
	v_rndne_f32_e32 v22, v15
	v_fmac_f32_e32 v19, 0xb2a5705f, v18
	v_sub_f32_e32 v15, v15, v22
	v_add_f32_e32 v15, v15, v19
	v_exp_f32_e32 v15, v15
	v_cvt_i32_f32_e32 v19, v22
	v_cmp_nlt_f32_e32 vcc, s6, v18
	v_add_f32_e32 v3, v3, v11
	v_ldexp_f32 v15, v15, v19
	v_cndmask_b32_e32 v15, 0, v15, vcc
	v_cmp_ngt_f32_e32 vcc, s7, v18
	s_nop 1
	v_cndmask_b32_e32 v15, v252, v15, vcc
	v_add_f32_e32 v15, 1.0, v15
	v_div_scale_f32 v18, s[4:5], v15, v15, 1.0
	v_rcp_f32_e32 v19, v18
	s_nop 0
	v_fma_f32 v22, -v18, v19, 1.0
	v_fmac_f32_e32 v19, v22, v19
	v_div_scale_f32 v22, vcc, 1.0, v15, 1.0
	v_mul_f32_e32 v23, v22, v19
	v_fma_f32 v36, -v18, v23, v22
	v_fmac_f32_e32 v23, v36, v19
	v_fma_f32 v18, -v18, v23, v22
	v_div_fmas_f32 v18, v18, v19, v23
	v_div_fixup_f32 v15, v18, v15, 1.0
	v_fma_f32 v18, -v24, v26, v34
	v_fma_f32 v16, v27, v18, v16
	v_fma_f32 v18, -v20, v26, v35
	v_fma_f32 v18, v27, v18, v12
	v_mul_f32_e32 v12, 0xbfb8aa3b, v16
	v_fma_f32 v19, v16, s3, -v12
	v_rndne_f32_e32 v20, v12
	v_fmac_f32_e32 v19, 0xb2a5705f, v16
	v_sub_f32_e32 v12, v12, v20
	v_add_f32_e32 v12, v12, v19
	v_exp_f32_e32 v12, v12
	v_cvt_i32_f32_e32 v19, v20
	v_cmp_nlt_f32_e32 vcc, s6, v16
	v_add_f32_e32 v7, v7, v15
	v_ldexp_f32 v12, v12, v19
	v_cndmask_b32_e32 v12, 0, v12, vcc
	v_cmp_ngt_f32_e32 vcc, s7, v16
	s_nop 1
	v_cndmask_b32_e32 v12, v252, v12, vcc
	v_add_f32_e32 v12, 1.0, v12
	v_div_scale_f32 v16, s[4:5], v12, v12, 1.0
	v_rcp_f32_e32 v19, v16
	s_nop 0
	v_fma_f32 v20, -v16, v19, 1.0
	v_fmac_f32_e32 v19, v20, v19
	v_div_scale_f32 v20, vcc, 1.0, v12, 1.0
	v_mul_f32_e32 v22, v20, v19
	v_fma_f32 v23, -v16, v22, v20
	v_fmac_f32_e32 v22, v23, v19
	v_fma_f32 v16, -v16, v22, v20
	v_div_fmas_f32 v16, v16, v19, v22
	v_div_fixup_f32 v12, v16, v12, 1.0
	v_mul_f32_e32 v16, 0xbfb8aa3b, v18
	v_fma_f32 v19, v18, s3, -v16
	v_rndne_f32_e32 v20, v16
	v_fmac_f32_e32 v19, 0xb2a5705f, v18
	v_sub_f32_e32 v16, v16, v20
	v_add_f32_e32 v16, v16, v19
	v_exp_f32_e32 v16, v16
	v_cvt_i32_f32_e32 v19, v20
	v_cmp_nlt_f32_e32 vcc, s6, v18
	v_add_f32_e32 v4, v4, v12
	v_ldexp_f32 v16, v16, v19
	v_cndmask_b32_e32 v16, 0, v16, vcc
	v_cmp_ngt_f32_e32 vcc, s7, v18
	s_nop 1
	v_cndmask_b32_e32 v16, v252, v16, vcc
	v_add_f32_e32 v16, 1.0, v16
	v_div_scale_f32 v18, s[4:5], v16, v16, 1.0
	v_rcp_f32_e32 v19, v18
	s_nop 0
	v_fma_f32 v20, -v18, v19, 1.0
	v_fmac_f32_e32 v19, v20, v19
	v_div_scale_f32 v20, vcc, 1.0, v16, 1.0
	v_mul_f32_e32 v22, v20, v19
	v_fma_f32 v23, -v18, v22, v20
	v_fmac_f32_e32 v22, v23, v19
	v_fma_f32 v18, -v18, v22, v20
	v_div_fmas_f32 v18, v18, v19, v22
	v_div_fixup_f32 v16, v18, v16, 1.0
	v_fma_f32 v18, -v25, v26, v32
	v_fmac_f32_e32 v17, v27, v18
	v_fma_f32 v18, -v21, v26, v33
	v_fmac_f32_e32 v13, v27, v18
	v_mul_f32_e32 v18, 0xbfb8aa3b, v17
	v_fma_f32 v19, v17, s3, -v18
	v_rndne_f32_e32 v20, v18
	v_fmac_f32_e32 v19, 0xb2a5705f, v17
	v_sub_f32_e32 v18, v18, v20
	v_add_f32_e32 v18, v18, v19
	v_exp_f32_e32 v18, v18
	v_cvt_i32_f32_e32 v19, v20
	v_cmp_nlt_f32_e32 vcc, s6, v17
	v_add_f32_e32 v8, v8, v16
	v_ldexp_f32 v18, v18, v19
	v_cndmask_b32_e32 v18, 0, v18, vcc
	v_cmp_ngt_f32_e32 vcc, s7, v17
	s_nop 1
	v_cndmask_b32_e32 v17, v252, v18, vcc
	v_add_f32_e32 v17, 1.0, v17
	v_div_scale_f32 v18, s[4:5], v17, v17, 1.0
	v_rcp_f32_e32 v19, v18
	s_nop 0
	v_fma_f32 v20, -v18, v19, 1.0
	v_fmac_f32_e32 v19, v20, v19
	v_div_scale_f32 v20, vcc, 1.0, v17, 1.0
	v_mul_f32_e32 v21, v20, v19
	v_fma_f32 v22, -v18, v21, v20
	v_fmac_f32_e32 v21, v22, v19
	v_fma_f32 v18, -v18, v21, v20
	v_div_fmas_f32 v18, v18, v19, v21
	v_div_fixup_f32 v17, v18, v17, 1.0
	v_mul_f32_e32 v18, 0xbfb8aa3b, v13
	v_fma_f32 v19, v13, s3, -v18
	v_rndne_f32_e32 v20, v18
	v_fmac_f32_e32 v19, 0xb2a5705f, v13
	v_sub_f32_e32 v18, v18, v20
	v_add_f32_e32 v18, v18, v19
	v_exp_f32_e32 v18, v18
	v_cvt_i32_f32_e32 v19, v20
	v_cmp_nlt_f32_e32 vcc, s6, v13
	v_ldexp_f32 v18, v18, v19
	s_nop 0
	v_cndmask_b32_e32 v18, 0, v18, vcc
	v_cmp_ngt_f32_e32 vcc, s7, v13
	s_nop 1
	v_cndmask_b32_e32 v13, v252, v18, vcc
	v_add_f32_e32 v13, 1.0, v13
	v_div_scale_f32 v18, s[4:5], v13, v13, 1.0
	v_rcp_f32_e32 v19, v18
	s_nop 0
	v_fma_f32 v20, -v18, v19, 1.0
	v_fmac_f32_e32 v19, v20, v19
	v_div_scale_f32 v20, vcc, 1.0, v13, 1.0
	v_mul_f32_e32 v21, v20, v19
	v_fma_f32 v22, -v18, v21, v20
	v_fmac_f32_e32 v21, v22, v19
	v_fma_f32 v18, -v18, v21, v20
	v_div_fmas_f32 v18, v18, v19, v21
	v_div_fixup_f32 v13, v18, v13, 1.0
	v_add_f32_e32 v18, v5, v17
	v_max_f32_e32 v5, v2, v3
	v_max_f32_e32 v20, v4, v18
	v_add_f32_e32 v9, v9, v13
	v_min_f32_e32 v19, v2, v3
	v_min_f32_e32 v22, v4, v18
	v_max_f32_e32 v21, v5, v20
	v_min_f32_e32 v5, v5, v20
	v_max3_f32 v23, v5, v19, v22
	v_max_f32_e32 v5, v6, v7
	v_max_f32_e32 v22, v8, v9
	v_min_f32_e32 v19, v6, v7
	v_min_f32_e32 v24, v8, v9
	v_max_f32_e32 v20, v5, v22
	v_min_f32_e32 v5, v5, v22
	v_max3_f32 v22, v5, v19, v24
	v_pk_add_f32 v[20:21], v[20:21], v[22:23]
	v_or_b32_e32 v5, 4, v31
	v_cmp_gt_f32_e32 vcc, v20, v21
	s_nop 1
	v_cndmask_b32_e32 v19, v21, v20, vcc
	v_and_b32_e32 v20, 64, v249
	v_add_u32_e32 v20, 64, v20
	v_xor_b32_e32 v21, 16, v249
	v_cndmask_b32_e32 v5, v31, v5, vcc
	v_cmp_lt_i32_e32 vcc, v21, v20
	s_nop 1
	v_cndmask_b32_e32 v21, v249, v21, vcc
	v_lshlrev_b32_e32 v22, 2, v21
	ds_bpermute_b32 v21, v22, v19
	ds_bpermute_b32 v22, v22, v5
	s_waitcnt lgkmcnt(1)
	v_cmp_lt_f32_e64 s[26:27], v19, v21
	v_cmp_nlt_f32_e32 vcc, v19, v21
	s_and_saveexec_b64 s[34:35], vcc
	s_cbranch_execz .LBB0_1044
	v_cmp_eq_f32_e32 vcc, v19, v21
	s_waitcnt lgkmcnt(0)
	v_cmp_lt_i32_e64 s[40:41], v22, v5
	s_and_b64 s[4:5], vcc, s[40:41]
	s_andn2_b64 s[6:7], s[26:27], exec
	s_and_b64 s[4:5], s[4:5], exec
	s_or_b64 s[26:27], s[6:7], s[4:5]
